# m1 + norm1(L1) gate-row loads batched (8 in flight) + final-norm g_final loads batched
# baseline (speedup 1.0000x reference)
; __device__ __forceinline__ float bflo(unsigned w) { return __uint_as_float(w << 16); }
; __device__ __forceinline__ float bfhi(unsigned w) { return __uint_as_float(w & 0xffff0000u); }
; __device__ __forceinline__ void phase_norm1(const Params& p, const Ctx& F, const int l) {
;     ...
;     for (; t < TPB; t += tstride) {
;         const bool isctx = t < CTXL;
;         const int mrow = isctx ? 8 : b;
;         const float* xs; float* xd; row_ptrs(p, F, l, b, t, xs, xd);
;         f32x4 v[8];
; #pragma unroll
;         for (int j = 0; j < 8; ++j) v[j] = vn[j] + (f32x4){bflo(dn[j].x), bfhi(dn[j].x), bflo(dn[j].y), bfhi(dn[j].y)};
;         if (comb) {
;             const float* gt = F.mod + (size_t)((l - 1) * 9 + mrow) * MODW + 5 * DM;
; #pragma unroll
;             for (int j = 0; j < 8; ++j) { v[j] += *((const f32x4*)gt + F.lane + 64 * j) * accn[j] * (1.f / Y_SCALE); if (!fin) *((f32x4*)xd + F.lane + 64 * j) = v[j]; }
;         }
.LBB0_157:
	v_readlane_b32 s14, v254, 31
	v_readlane_b32 s15, v254, 32
	s_and_b64 s[0:1], s[0:1], exec
	v_lshlrev_b32_e32 v132, 16, v164
	v_and_b32_e32 v133, 0xffff0000, v164
	v_lshlrev_b32_e32 v134, 16, v165
	v_and_b32_e32 v135, 0xffff0000, v165
	v_lshlrev_b32_e32 v136, 16, v166
	v_and_b32_e32 v137, 0xffff0000, v166
	v_lshlrev_b32_e32 v138, 16, v167
	v_and_b32_e32 v139, 0xffff0000, v167
	v_lshlrev_b32_e32 v140, 16, v168
	v_and_b32_e32 v141, 0xffff0000, v168
	v_lshlrev_b32_e32 v142, 16, v169
	v_and_b32_e32 v143, 0xffff0000, v169
	v_lshlrev_b32_e32 v144, 16, v170
	v_and_b32_e32 v145, 0xffff0000, v170
	v_lshlrev_b32_e32 v146, 16, v171
	v_and_b32_e32 v147, 0xffff0000, v171
	v_lshlrev_b32_e32 v148, 16, v172
	v_and_b32_e32 v149, 0xffff0000, v172
	v_lshlrev_b32_e32 v150, 16, v173
	v_and_b32_e32 v151, 0xffff0000, v173
	v_lshlrev_b32_e32 v152, 16, v176
	v_and_b32_e32 v153, 0xffff0000, v176
	v_lshlrev_b32_e32 v154, 16, v177
	v_and_b32_e32 v155, 0xffff0000, v177
	v_lshlrev_b32_e32 v156, 16, v178
	v_and_b32_e32 v157, 0xffff0000, v178
	v_lshlrev_b32_e32 v158, 16, v179
	v_and_b32_e32 v159, 0xffff0000, v179
	v_lshlrev_b32_e32 v160, 16, v174
	v_and_b32_e32 v161, 0xffff0000, v174
	v_lshlrev_b32_e32 v162, 16, v175
	v_and_b32_e32 v163, 0xffff0000, v175
	v_cndmask_b32_e64 v1, 0, 1, s[14:15]
	s_cselect_b32 s30, 8, s19
	s_waitcnt vmcnt(7)
	v_pk_add_f32 v[134:135], v[38:39], v[134:135]
	v_pk_add_f32 v[132:133], v[36:37], v[132:133]
	s_waitcnt vmcnt(6)
	v_pk_add_f32 v[138:139], v[42:43], v[138:139]
	v_pk_add_f32 v[136:137], v[40:41], v[136:137]
	s_waitcnt vmcnt(5)
	v_pk_add_f32 v[142:143], v[46:47], v[142:143]
	v_pk_add_f32 v[140:141], v[44:45], v[140:141]
	s_waitcnt vmcnt(4)
	v_pk_add_f32 v[146:147], v[50:51], v[146:147]
	v_pk_add_f32 v[144:145], v[48:49], v[144:145]
	s_waitcnt vmcnt(3)
	v_pk_add_f32 v[150:151], v[54:55], v[150:151]
	v_pk_add_f32 v[148:149], v[52:53], v[148:149]
	s_waitcnt vmcnt(2)
	v_pk_add_f32 v[154:155], v[58:59], v[154:155]
	v_pk_add_f32 v[152:153], v[56:57], v[152:153]
	s_waitcnt vmcnt(1)
	v_pk_add_f32 v[158:159], v[62:63], v[158:159]
	v_pk_add_f32 v[156:157], v[60:61], v[156:157]
	s_waitcnt vmcnt(0)
	v_pk_add_f32 v[162:163], v[66:67], v[162:163]
	v_cmp_ne_u32_e64 s[0:1], 1, v1
	s_andn2_b64 vcc, exec, s[14:15]
	v_pk_add_f32 v[160:161], v[64:65], v[160:161]
	s_cbranch_vccnz .LBB0_159
	s_lshl_b64 s[2:3], s[2:3], 13
	s_add_u32 s2, s12, s2
	s_addc_u32 s3, s13, s3
	s_add_i32 s12, s23, s30
	s_mul_hi_u32 s13, s12, 0xc000
	s_mul_i32 s12, s12, 0xc000
	s_add_u32 s12, s24, s12
	s_addc_u32 s13, s25, s13
	v_lshl_add_u64 v[198:199], s[12:13], 0, v[34:35]
	s_mov_b32 s12, 0xb000
	v_add_co_u32_e32 v200, vcc, s12, v198
	s_mov_b64 s[12:13], 0xa000
	s_nop 0
	v_addc_co_u32_e32 v201, vcc, 0, v199, vcc
	v_lshl_add_u64 v[198:199], v[198:199], 0, s[12:13]
	global_load_dwordx4 v[210:213], v[200:201], off offset:-4096
	global_load_dwordx4 v[224:227], v[198:199], off offset:1024
	global_load_dwordx4 v[228:231], v[198:199], off offset:2048
	global_load_dwordx4 v[232:235], v[198:199], off offset:3072
	global_load_dwordx4 v[236:239], v[200:201], off
	global_load_dwordx4 v[240:243], v[200:201], off offset:1024
	global_load_dwordx4 v[244:247], v[200:201], off offset:2048
	global_load_dwordx4 v[248:251], v[200:201], off offset:3072
	s_mov_b32 s12, 0x3d000000
	s_waitcnt vmcnt(7)
	v_pk_mul_f32 v[212:213], v[4:5], v[212:213]
	v_pk_mul_f32 v[210:211], v[2:3], v[210:211]
	v_pk_fma_f32 v[134:135], v[212:213], s[12:13], v[134:135] op_sel_hi:[1,0,1]
	v_pk_fma_f32 v[132:133], v[210:211], s[12:13], v[132:133] op_sel_hi:[1,0,1]
	global_store_dwordx4 v34, v[132:135], s[2:3]
	s_waitcnt vmcnt(7)
	v_pk_mul_f32 v[226:227], v[8:9], v[226:227]
	v_pk_mul_f32 v[224:225], v[6:7], v[224:225]
	v_pk_fma_f32 v[138:139], v[226:227], s[12:13], v[138:139] op_sel_hi:[1,0,1]
	v_pk_fma_f32 v[136:137], v[224:225], s[12:13], v[136:137] op_sel_hi:[1,0,1]
	global_store_dwordx4 v34, v[136:139], s[2:3] offset:1024
	s_waitcnt vmcnt(7)
	v_pk_mul_f32 v[230:231], v[12:13], v[230:231]
	v_pk_mul_f32 v[228:229], v[10:11], v[228:229]
	v_pk_fma_f32 v[142:143], v[230:231], s[12:13], v[142:143] op_sel_hi:[1,0,1]
	v_pk_fma_f32 v[140:141], v[228:229], s[12:13], v[140:141] op_sel_hi:[1,0,1]
	global_store_dwordx4 v34, v[140:143], s[2:3] offset:2048
	s_waitcnt vmcnt(7)
	v_pk_mul_f32 v[234:235], v[16:17], v[234:235]
	v_pk_mul_f32 v[232:233], v[14:15], v[232:233]
	v_pk_fma_f32 v[146:147], v[234:235], s[12:13], v[146:147] op_sel_hi:[1,0,1]
	v_pk_fma_f32 v[144:145], v[232:233], s[12:13], v[144:145] op_sel_hi:[1,0,1]
	global_store_dwordx4 v34, v[144:147], s[2:3] offset:3072
	v_lshl_add_u64 v[198:199], s[2:3], 0, v[34:35]
	v_add_co_u32_e32 v198, vcc, 0x1000, v198
	s_nop 1
	v_addc_co_u32_e32 v199, vcc, 0, v199, vcc
	s_waitcnt vmcnt(7)
	v_pk_mul_f32 v[238:239], v[20:21], v[238:239]
	v_pk_mul_f32 v[236:237], v[18:19], v[236:237]
	v_pk_fma_f32 v[150:151], v[238:239], s[12:13], v[150:151] op_sel_hi:[1,0,1]
	v_pk_fma_f32 v[148:149], v[236:237], s[12:13], v[148:149] op_sel_hi:[1,0,1]
	global_store_dwordx4 v[198:199], v[148:151], off
	s_waitcnt vmcnt(7)
	v_pk_mul_f32 v[242:243], v[24:25], v[242:243]
	v_pk_mul_f32 v[240:241], v[22:23], v[240:241]
	v_pk_fma_f32 v[154:155], v[242:243], s[12:13], v[154:155] op_sel_hi:[1,0,1]
	v_pk_fma_f32 v[152:153], v[240:241], s[12:13], v[152:153] op_sel_hi:[1,0,1]
	global_store_dwordx4 v[198:199], v[152:155], off offset:1024
	s_waitcnt vmcnt(7)
	v_pk_mul_f32 v[246:247], v[28:29], v[246:247]
	v_pk_mul_f32 v[244:245], v[26:27], v[244:245]
	v_pk_fma_f32 v[158:159], v[246:247], s[12:13], v[158:159] op_sel_hi:[1,0,1]
	v_pk_fma_f32 v[156:157], v[244:245], s[12:13], v[156:157] op_sel_hi:[1,0,1]
	global_store_dwordx4 v[198:199], v[156:159], off offset:2048
	s_waitcnt vmcnt(7)
	v_pk_mul_f32 v[250:251], v[32:33], v[250:251]
	v_pk_mul_f32 v[248:249], v[30:31], v[248:249]
	v_pk_fma_f32 v[162:163], v[250:251], s[12:13], v[162:163] op_sel_hi:[1,0,1]
	v_pk_fma_f32 v[160:161], v[248:249], s[12:13], v[160:161] op_sel_hi:[1,0,1]
	global_store_dwordx4 v[198:199], v[160:163], off offset:3072

; __device__ __forceinline__ float bflo(unsigned w) { return __uint_as_float(w << 16); }
; __device__ __forceinline__ float bfhi(unsigned w) { return __uint_as_float(w & 0xffff0000u); }
; __device__ __forceinline__ void phase_norm1(const Params& p, const Ctx& F, const int l) {
;     ...
;         for (int j = 0; j < 8; ++j) v[j] = vn[j] + (f32x4){bflo(dn[j].x), bfhi(dn[j].x), bflo(dn[j].y), bfhi(dn[j].y)};
;         if (comb) {
;             const float* gt = F.mod + (size_t)((l - 1) * 9 + mrow) * MODW + 5 * DM;
; #pragma unroll
;             for (int j = 0; j < 8; ++j) { v[j] += *((const f32x4*)gt + F.lane + 64 * j) * accn[j] * (1.f / Y_SCALE); if (!fin) *((f32x4*)xd + F.lane + 64 * j) = v[j]; }
;         }
;         { const int t2 = t + tstride;
;           if (t2 < TPB) { const float* xs2; float* xd2; row_ptrs(p, F, l, b, t2, xs2, xd2);
; #pragma unroll
;             for (int j = 0; j < 8; ++j) vn[j] = __builtin_nontemporal_load((const f32x4*)xs2 + F.lane + 64 * j);
;             if (comb) {
; #pragma unroll
;                 for (int j = 0; j < 8; ++j) dn[j] = __builtin_nontemporal_load((const u32x2*)(F.dlt + ((size_t)b * TPB + t2) * DM + 4 * F.lane + 256 * j)); }
;             if (comb) { { if (fin) gather_y1(F, sn, accn); else gather_y(F, sn, accn); } const int t3 = t2 + tstride; sn = -1; if (t3 < TPB && F.lane < 16) sn = F.slot[(unsigned)((b * 16 + F.lane) * TPB + t3)]; } } }
;         if (mrow != cur_m) { cur_m = mrow;
;             if (!fin) {
;                 const float* mr = F.mod + (size_t)(l * 9 + mrow) * MODW;
; #pragma unroll
;                 for (int j = 0; j < 8; ++j) { const f32x4 g = *((const f32x4*)(p.g_mix + l * DM) + F.lane + 64 * j), sc = *((const f32x4*)(mr + DM) + F.lane + 64 * j);
;                     A[j] = g * (sc + 1.f); Bv[j] = *((const f32x4*)mr + F.lane + 64 * j); }
;             }
;         }
;         float ss = 0.f;
; #pragma unroll
;         for (int j = 0; j < 8; ++j) ss += (v[j].x * v[j].x + v[j].y * v[j].y) + (v[j].z * v[j].z + v[j].w * v[j].w);
;         const float rstd = rsqrtf(wave_sum(ss) * (1.f / DM) + EPS);
;         if (fin) {
; #pragma unroll
;             for (int j = 0; j < 8; ++j) __builtin_nontemporal_store(v[j] * rstd * *((const f32x4*)p.g_final + F.lane + 64 * j), (f32x4*)xd + F.lane + 64 * j);
.LBB0_1459:
	v_lshlrev_b32_e32 v96, 16, v146
	v_and_b32_e32 v97, 0xffff0000, v146
	v_lshlrev_b32_e32 v98, 16, v147
	v_and_b32_e32 v99, 0xffff0000, v147
	v_pk_add_f32 v[28:29], v[28:29], v[96:97]
	v_pk_add_f32 v[30:31], v[30:31], v[98:99]
	v_lshlrev_b32_e32 v96, 16, v144
	v_and_b32_e32 v97, 0xffff0000, v144
	v_lshlrev_b32_e32 v98, 16, v145
	v_and_b32_e32 v99, 0xffff0000, v145
	v_pk_add_f32 v[24:25], v[24:25], v[96:97]
	v_pk_add_f32 v[26:27], v[26:27], v[98:99]
	v_lshlrev_b32_e32 v96, 16, v142
	v_and_b32_e32 v97, 0xffff0000, v142
	v_lshlrev_b32_e32 v98, 16, v143
	v_and_b32_e32 v99, 0xffff0000, v143
	v_pk_add_f32 v[20:21], v[20:21], v[96:97]
	v_pk_add_f32 v[22:23], v[22:23], v[98:99]
	v_lshlrev_b32_e32 v96, 16, v140
	v_and_b32_e32 v97, 0xffff0000, v140
	v_lshlrev_b32_e32 v98, 16, v141
	v_and_b32_e32 v99, 0xffff0000, v141
	v_pk_add_f32 v[16:17], v[16:17], v[96:97]
	v_pk_add_f32 v[18:19], v[18:19], v[98:99]
	v_lshlrev_b32_e32 v96, 16, v138
	v_and_b32_e32 v97, 0xffff0000, v138
	v_lshlrev_b32_e32 v98, 16, v139
	v_and_b32_e32 v99, 0xffff0000, v139
	v_pk_add_f32 v[12:13], v[12:13], v[96:97]
	v_pk_add_f32 v[14:15], v[14:15], v[98:99]
	v_lshlrev_b32_e32 v96, 16, v136
	v_and_b32_e32 v97, 0xffff0000, v136
	v_lshlrev_b32_e32 v98, 16, v137
	v_and_b32_e32 v99, 0xffff0000, v137
	v_pk_add_f32 v[96:97], v[8:9], v[96:97]
	v_pk_add_f32 v[8:9], v[10:11], v[98:99]
	v_lshlrev_b32_e32 v10, 16, v134
	v_and_b32_e32 v11, 0xffff0000, v134
	v_lshlrev_b32_e32 v98, 16, v135
	v_and_b32_e32 v99, 0xffff0000, v135
	v_pk_add_f32 v[100:101], v[4:5], v[10:11]
	v_lshlrev_b32_e32 v4, 16, v132
	v_and_b32_e32 v5, 0xffff0000, v132
	v_pk_add_f32 v[98:99], v[6:7], v[98:99]
	v_lshlrev_b32_e32 v6, 16, v133
	v_and_b32_e32 v7, 0xffff0000, v133
	v_pk_add_f32 v[102:103], v[0:1], v[4:5]
	s_waitcnt vmcnt(5)
	v_pk_mul_f32 v[0:1], v[154:155], v[94:95]
	v_pk_add_f32 v[104:105], v[2:3], v[6:7]
	v_pk_mul_f32 v[2:3], v[148:149], v[92:93]
	v_pk_fma_f32 v[30:31], v[0:1], s[12:13], v[30:31] op_sel_hi:[1,0,1]
	v_pk_mul_f32 v[0:1], v[156:157], v[90:91]
	v_pk_fma_f32 v[28:29], v[2:3], s[12:13], v[28:29] op_sel_hi:[1,0,1]
	v_pk_mul_f32 v[2:3], v[150:151], v[88:89]
	v_pk_fma_f32 v[26:27], v[0:1], s[12:13], v[26:27] op_sel_hi:[1,0,1]
	v_pk_mul_f32 v[0:1], v[160:161], v[86:87]
	v_pk_fma_f32 v[24:25], v[2:3], s[12:13], v[24:25] op_sel_hi:[1,0,1]
	v_pk_mul_f32 v[2:3], v[152:153], v[84:85]
	v_pk_fma_f32 v[22:23], v[0:1], s[12:13], v[22:23] op_sel_hi:[1,0,1]
	s_waitcnt vmcnt(4)
	v_pk_mul_f32 v[0:1], v[164:165], v[82:83]
	v_pk_fma_f32 v[20:21], v[2:3], s[12:13], v[20:21] op_sel_hi:[1,0,1]
	v_pk_mul_f32 v[2:3], v[158:159], v[80:81]
	v_pk_fma_f32 v[18:19], v[0:1], s[12:13], v[18:19] op_sel_hi:[1,0,1]
	s_waitcnt vmcnt(3)
	v_pk_mul_f32 v[0:1], v[168:169], v[78:79]
	v_pk_fma_f32 v[16:17], v[2:3], s[12:13], v[16:17] op_sel_hi:[1,0,1]
	v_pk_mul_f32 v[2:3], v[162:163], v[76:77]
	v_pk_fma_f32 v[4:5], v[0:1], s[12:13], v[14:15] op_sel_hi:[1,0,1]
	s_waitcnt vmcnt(0)
	v_pk_mul_f32 v[14:15], v[174:175], v[64:65]
	v_pk_fma_f32 v[6:7], v[2:3], s[12:13], v[12:13] op_sel_hi:[1,0,1]
	v_pk_mul_f32 v[2:3], v[166:167], v[72:73]
	v_pk_mul_f32 v[12:13], v[178:179], v[66:67]
	v_pk_fma_f32 v[66:67], v[14:15], s[12:13], v[102:103] op_sel_hi:[1,0,1]
	v_mov_b32_e32 v14, v29
	v_mov_b32_e32 v15, v25
	v_pk_fma_f32 v[10:11], v[2:3], s[12:13], v[96:97] op_sel_hi:[1,0,1]
	v_pk_mul_f32 v[2:3], v[170:171], v[68:69]
	v_pk_fma_f32 v[64:65], v[12:13], s[12:13], v[104:105] op_sel_hi:[1,0,1]
	v_mov_b32_e32 v12, v28
	v_mov_b32_e32 v13, v24
	v_pk_mul_f32 v[14:15], v[14:15], v[14:15]
	v_mov_b32_e32 v68, v31
	v_mov_b32_e32 v69, v27
	v_pk_fma_f32 v[12:13], v[12:13], v[12:13], v[14:15]
	v_mov_b32_e32 v14, v30
	v_mov_b32_e32 v15, v26
	v_pk_mul_f32 v[68:69], v[68:69], v[68:69]
	v_pk_mul_f32 v[0:1], v[172:173], v[74:75]
	v_pk_fma_f32 v[14:15], v[14:15], v[14:15], v[68:69]
	v_pk_mul_f32 v[68:69], v[20:21], v[20:21]
	v_pk_add_f32 v[12:13], v[12:13], v[14:15]
	v_pk_mul_f32 v[14:15], v[22:23], v[22:23]
	v_pk_fma_f32 v[8:9], v[0:1], s[12:13], v[8:9] op_sel_hi:[1,0,1]
	v_pk_mul_f32 v[0:1], v[176:177], v[70:71]
	v_pk_mov_b32 v[70:71], v[68:69], v[14:15] op_sel:[1,0]
	v_mov_b32_e32 v69, v15
	v_pk_add_f32 v[14:15], v[70:71], v[68:69]
	v_mul_f32_e32 v68, v6, v6
	v_mul_f32_e32 v69, v7, v7
	v_pk_add_f32 v[12:13], v[12:13], v[12:13] op_sel:[0,1] op_sel_hi:[1,0]
	v_pk_add_f32 v[14:15], v[14:15], v[14:15] op_sel:[0,1] op_sel_hi:[1,0]
	v_mov_b32_e32 v13, v68
	v_mov_b32_e32 v15, v69
	v_pk_add_f32 v[68:69], v[12:13], v[14:15]
	global_load_dwordx4 v[12:15], v[180:181], off
	global_load_dwordx4 v[76:79], v[180:181], off offset:1024
	global_load_dwordx4 v[80:83], v[180:181], off offset:2048
	global_load_dwordx4 v[84:87], v[180:181], off offset:3072
	global_load_dwordx4 v[88:91], v[182:183], off
	global_load_dwordx4 v[92:95], v[184:185], off
	global_load_dwordx4 v[108:111], v[186:187], off
	global_load_dwordx4 v[112:115], v[188:189], off
	v_mul_f32_e32 v70, v17, v17
	v_mul_f32_e32 v72, v4, v4
	v_pk_fma_f32 v[70:71], v[16:17], v[16:17], v[70:71] op_sel_hi:[1,1,0]
	v_mul_f32_e32 v74, v5, v5
	v_mov_b32_e32 v71, v72
	v_mul_f32_e32 v72, v19, v19
	v_pk_fma_f32 v[72:73], v[18:19], v[18:19], v[72:73] op_sel_hi:[1,1,0]
	v_pk_fma_f32 v[0:1], v[0:1], s[12:13], v[98:99] op_sel_hi:[1,0,1]
	v_mov_b32_e32 v73, v74
	v_pk_add_f32 v[70:71], v[70:71], v[72:73]
	v_pk_mul_f32 v[72:73], v[10:11], v[10:11]
	v_pk_add_f32 v[68:69], v[68:69], v[70:71]
	v_pk_mul_f32 v[70:71], v[8:9], v[8:9]
	v_pk_add_f32 v[68:69], v[68:69], v[68:69] op_sel:[0,1] op_sel_hi:[1,0]
	v_pk_mov_b32 v[74:75], v[72:73], v[70:71] op_sel:[1,0]
	v_mov_b32_e32 v73, v71
	v_pk_add_f32 v[70:71], v[74:75], v[72:73]
	v_mul_f32_e32 v72, v66, v66
	v_mul_f32_e32 v73, v67, v67
	v_pk_add_f32 v[70:71], v[70:71], v[70:71] op_sel:[0,1] op_sel_hi:[1,0]
	v_pk_fma_f32 v[2:3], v[2:3], s[12:13], v[100:101] op_sel_hi:[1,0,1]
	v_mov_b32_e32 v69, v72
	v_mov_b32_e32 v71, v73
	v_pk_add_f32 v[68:69], v[68:69], v[70:71]
	v_mul_f32_e32 v70, v3, v3
	v_mul_f32_e32 v72, v1, v1
	v_mul_f32_e32 v74, v64, v64
	v_mul_f32_e32 v75, v65, v65
	v_pk_fma_f32 v[70:71], v[2:3], v[2:3], v[70:71] op_sel_hi:[1,1,0]
	v_pk_fma_f32 v[72:73], v[0:1], v[0:1], v[72:73] op_sel_hi:[1,1,0]
	v_mov_b32_e32 v71, v74
	v_mov_b32_e32 v73, v75
	v_pk_add_f32 v[70:71], v[70:71], v[72:73]
	s_lshl_b64 s[16:17], s[16:17], 13
	v_pk_add_f32 v[68:69], v[68:69], v[70:71]
	s_add_u32 s16, s18, s16
	v_add_f32_e32 v68, v68, v69
	ds_bpermute_b32 v69, v209, v68
	s_addc_u32 s17, s19, s17
	v_mov_b64_e32 v[132:133], v[206:207]
	v_mov_b64_e32 v[134:135], v[204:205]
	v_mov_b64_e32 v[136:137], v[202:203]
	s_waitcnt lgkmcnt(0)
; __device__ __forceinline__ void phase_norm1(const Params& p, const Ctx& F, const int l) {
;     ...
;         float ss = 0.f;
; #pragma unroll
;         for (int j = 0; j < 8; ++j) ss += (v[j].x * v[j].x + v[j].y * v[j].y) + (v[j].z * v[j].z + v[j].w * v[j].w);
;         const float rstd = rsqrtf(wave_sum(ss) * (1.f / DM) + EPS);
;         if (fin) {
; #pragma unroll
;             for (int j = 0; j < 8; ++j) __builtin_nontemporal_store(v[j] * rstd * *((const f32x4*)p.g_final + F.lane + 64 * j), (f32x4*)xd + F.lane + 64 * j);
	v_add_f32_e32 v68, v68, v69
	ds_bpermute_b32 v69, v210, v68
	v_mov_b64_e32 v[138:139], v[200:201]
	v_mov_b64_e32 v[140:141], v[198:199]
	v_mov_b64_e32 v[142:143], v[196:197]
	v_mov_b64_e32 v[144:145], v[194:195]
	s_waitcnt lgkmcnt(0)
	v_add_f32_e32 v68, v68, v69
	ds_bpermute_b32 v69, v211, v68
	v_mov_b64_e32 v[146:147], v[192:193]
	v_mov_b32_e32 v148, v217
	v_mov_b32_e32 v149, v218
	v_mov_b32_e32 v154, v219
	s_waitcnt lgkmcnt(0)
	v_add_f32_e32 v68, v68, v69
	ds_bpermute_b32 v69, v212, v68
	v_mov_b32_e32 v155, v220
	v_mov_b32_e32 v150, v221
	v_mov_b32_e32 v151, v222
	v_mov_b32_e32 v156, v223
	s_waitcnt lgkmcnt(0)
	v_add_f32_e32 v68, v68, v69
	ds_bpermute_b32 v69, v213, v68
	v_mov_b32_e32 v157, v224
	v_mov_b32_e32 v152, v225
	v_mov_b32_e32 v153, v226
	v_mov_b32_e32 v160, v227
	s_waitcnt lgkmcnt(0)
	v_add_f32_e32 v68, v68, v69
	ds_bpermute_b32 v69, v214, v68
	v_mov_b32_e32 v161, v228
	v_mov_b32_e32 v158, v229
	v_mov_b32_e32 v159, v230
	v_mov_b32_e32 v164, v231
	s_waitcnt lgkmcnt(0)
	v_add_f32_e32 v68, v68, v69
	v_fmamk_f32 v68, v68, 0x3a000000, v216
	v_mul_f32_e32 v69, 0x4b800000, v68
	v_cmp_gt_f32_e32 vcc, s31, v68
	v_mov_b32_e32 v165, v232
	v_mov_b32_e32 v162, v233
	v_cndmask_b32_e32 v68, v68, v69, vcc
	v_rsq_f32_e32 v68, v68
	v_mov_b32_e32 v163, v235
	v_mov_b32_e32 v168, v236
	v_mov_b32_e32 v169, v237
	v_mul_f32_e32 v69, 0x45800000, v68
	v_cndmask_b32_e32 v72, v68, v69, vcc
	v_pk_mul_f32 v[28:29], v[28:29], v[72:73] op_sel_hi:[1,0]
	v_pk_mul_f32 v[30:31], v[30:31], v[72:73] op_sel_hi:[1,0]
	s_waitcnt vmcnt(7)
	v_pk_mul_f32 v[12:13], v[12:13], v[28:29]
	v_pk_mul_f32 v[14:15], v[14:15], v[30:31]
	global_store_dwordx4 v128, v[12:15], s[16:17] nt
	v_pk_mul_f32 v[26:27], v[26:27], v[72:73] op_sel_hi:[1,0]
	v_pk_mul_f32 v[24:25], v[24:25], v[72:73] op_sel_hi:[1,0]
	v_pk_mul_f32 v[22:23], v[22:23], v[72:73] op_sel_hi:[1,0]
	v_pk_mul_f32 v[20:21], v[20:21], v[72:73] op_sel_hi:[1,0]
	v_pk_mul_f32 v[18:19], v[18:19], v[72:73] op_sel_hi:[1,0]
	v_pk_mul_f32 v[16:17], v[16:17], v[72:73] op_sel_hi:[1,0]
	v_pk_mul_f32 v[8:9], v[8:9], v[72:73] op_sel_hi:[1,0]
	v_pk_mul_f32 v[10:11], v[10:11], v[72:73] op_sel_hi:[1,0]
	v_mov_b64_e32 v[28:29], v[32:33]
	v_mov_b64_e32 v[30:31], v[34:35]
	v_pk_mul_f32 v[34:35], v[64:65], v[72:73] op_sel_hi:[1,0]
	v_pk_mul_f32 v[32:33], v[66:67], v[72:73] op_sel_hi:[1,0]
	v_mov_b32_e32 v166, v238
	v_mov_b32_e32 v167, v239
	v_mov_b32_e32 v172, v240
	v_mov_b32_e32 v173, v241
	v_mov_b32_e32 v170, v242
	v_mov_b32_e32 v171, v243
	v_mov_b32_e32 v176, v244
	v_mov_b32_e32 v177, v245
	v_mov_b32_e32 v174, v246
	v_mov_b32_e32 v175, v247
	v_mov_b32_e32 v178, v248
	v_mov_b32_e32 v179, v234
	s_waitcnt vmcnt(7)
	v_pk_mul_f32 v[76:77], v[76:77], v[24:25]
	v_pk_mul_f32 v[78:79], v[78:79], v[26:27]
	global_store_dwordx4 v128, v[76:79], s[16:17] offset:1024 nt
	v_mov_b64_e32 v[24:25], v[36:37]
	v_mov_b64_e32 v[26:27], v[38:39]
	s_waitcnt vmcnt(7)
	v_pk_mul_f32 v[80:81], v[80:81], v[20:21]
	v_pk_mul_f32 v[82:83], v[82:83], v[22:23]
	global_store_dwordx4 v128, v[80:83], s[16:17] offset:2048 nt
	v_mov_b64_e32 v[20:21], v[40:41]
	v_mov_b64_e32 v[22:23], v[42:43]
	s_waitcnt vmcnt(7)
	v_pk_mul_f32 v[84:85], v[84:85], v[16:17]
	v_pk_mul_f32 v[86:87], v[86:87], v[18:19]
	global_store_dwordx4 v128, v[84:87], s[16:17] offset:3072 nt
	v_lshl_add_u64 v[16:17], s[16:17], 0, v[128:129]
	v_add_co_u32_e32 v74, vcc, s30, v16
	s_nop 1
	v_addc_co_u32_e32 v75, vcc, 0, v17, vcc
	v_pk_mul_f32 v[16:17], v[4:5], v[72:73] op_sel_hi:[1,0]
	v_pk_mul_f32 v[4:5], v[6:7], v[72:73] op_sel_hi:[1,0]
	s_andn2_b64 vcc, exec, s[14:15]
	s_waitcnt vmcnt(7)
	v_pk_mul_f32 v[4:5], v[88:89], v[4:5]
	v_pk_mul_f32 v[6:7], v[90:91], v[16:17]
	global_store_dwordx4 v[74:75], v[4:7], off nt
	v_mov_b64_e32 v[12:13], v[48:49]
	v_mov_b64_e32 v[16:17], v[44:45]
	v_mov_b64_e32 v[14:15], v[50:51]
	v_mov_b64_e32 v[18:19], v[46:47]
	s_waitcnt vmcnt(7)
	v_pk_mul_f32 v[4:5], v[92:93], v[10:11]
	v_pk_mul_f32 v[6:7], v[94:95], v[8:9]
	global_store_dwordx4 v[74:75], v[4:7], off offset:1024 nt
	v_pk_mul_f32 v[8:9], v[0:1], v[72:73] op_sel_hi:[1,0]
	v_pk_mul_f32 v[0:1], v[2:3], v[72:73] op_sel_hi:[1,0]
	s_waitcnt vmcnt(7)
	v_pk_mul_f32 v[2:3], v[8:9], v[110:111]
	v_pk_mul_f32 v[0:1], v[0:1], v[108:109]
	global_store_dwordx4 v[74:75], v[0:3], off offset:2048 nt
	s_nop 1
	v_mov_b64_e32 v[4:5], v[56:57]
	v_mov_b64_e32 v[0:1], v[60:61]
	v_mov_b64_e32 v[8:9], v[52:53]
	v_mov_b64_e32 v[2:3], v[62:63]
	v_mov_b64_e32 v[6:7], v[58:59]
	v_mov_b64_e32 v[10:11], v[54:55]
	s_waitcnt vmcnt(7)
	v_pk_mul_f32 v[32:33], v[32:33], v[112:113]
	v_pk_mul_f32 v[34:35], v[34:35], v[114:115]
	global_store_dwordx4 v[74:75], v[32:35], off offset:3072 nt
	s_cbranch_vccz .LBB0_1478
